# attention tile loops: running-max registers swap roles between the two unrolled copies, the two per-tile loop-head v_mov copies removed
# speedup vs baseline: 1.0015x; 1.0015x over previous
.LBB0_1254:
	s_and_b32 s34, s31, 1
	s_cmp_lt_i32 s31, s29
	s_mov_b64 s[18:19], -1
	s_cbranch_scc1 .LBB0_1256

.Lat0_O_1258:
	ds_read_b128 v[102:105], v222 offset:16384
	ds_read_b128 v[106:109], v223 offset:16384
	ds_read_b128 v[110:113], v224 offset:16384
	ds_read_b128 v[114:117], v225 offset:16384
	ds_read_b128 v[118:121], v222 offset:20480
	ds_read_b128 v[122:125], v223 offset:20480
	ds_read_b128 v[126:129], v224 offset:20480
	ds_read_b128 v[130:133], v225 offset:20480
	s_waitcnt lgkmcnt(0)
	v_mfma_f32_16x16x32_bf16 v[138:141], v[118:121], v[78:81], 0
	v_mfma_f32_16x16x32_bf16 v[134:137], v[102:105], v[78:81], 0
	v_mfma_f32_16x16x32_bf16 v[102:105], v[102:105], v[94:97], 0
	v_mfma_f32_16x16x32_bf16 v[118:121], v[118:121], v[94:97], 0
	v_mfma_f32_16x16x32_bf16 v[134:137], v[106:109], v[70:73], v[134:137]
	v_mfma_f32_16x16x32_bf16 v[102:105], v[106:109], v[86:89], v[102:105]
	v_mfma_f32_16x16x32_bf16 v[138:141], v[122:125], v[70:73], v[138:141]
	v_mfma_f32_16x16x32_bf16 v[118:121], v[122:125], v[86:89], v[118:121]
	v_mfma_f32_16x16x32_bf16 v[134:137], v[110:113], v[74:77], v[134:137]
	v_mfma_f32_16x16x32_bf16 v[102:105], v[110:113], v[90:93], v[102:105]
	v_mfma_f32_16x16x32_bf16 v[138:141], v[126:129], v[74:77], v[138:141]
	v_mfma_f32_16x16x32_bf16 v[118:121], v[126:129], v[90:93], v[118:121]
	v_mfma_f32_16x16x32_bf16 v[162:165], v[114:117], v[82:85], v[134:137]
	v_mfma_f32_16x16x32_bf16 v[134:137], v[114:117], v[98:101], v[102:105]
	s_nop 3
	ds_read_b128 v[102:105], v222 offset:24576
	ds_read_b128 v[106:109], v223 offset:24576
	ds_read_b128 v[110:113], v224 offset:24576
	ds_read_b128 v[114:117], v225 offset:24576
	v_max_f32_e32 v218, v164, v165
	v_mfma_f32_16x16x32_bf16 v[158:161], v[130:133], v[82:85], v[138:141]
	v_max3_f32 v218, v162, v163, v218
	v_mfma_f32_16x16x32_bf16 v[138:141], v[130:133], v[98:101], v[118:121]
	s_nop 2
	ds_read_b128 v[118:121], v222 offset:28672
	ds_read_b128 v[122:125], v223 offset:28672
	ds_read_b128 v[126:129], v224 offset:28672
	ds_read_b128 v[130:133], v225 offset:28672
	v_max3_f32 v189, v159, v160, v161
	v_max3_f32 v218, v218, v158, v189
	s_waitcnt lgkmcnt(0)
	v_mfma_f32_16x16x32_bf16 v[142:145], v[102:105], v[78:81], 0
	v_mfma_f32_16x16x32_bf16 v[102:105], v[102:105], v[94:97], 0
	v_mfma_f32_16x16x32_bf16 v[102:105], v[106:109], v[86:89], v[102:105]
	v_mfma_f32_16x16x32_bf16 v[102:105], v[110:113], v[90:93], v[102:105]
	v_mfma_f32_16x16x32_bf16 v[146:149], v[114:117], v[98:101], v[102:105]
	v_mfma_f32_16x16x32_bf16 v[102:105], v[118:121], v[78:81], 0
	v_mfma_f32_16x16x32_bf16 v[142:145], v[106:109], v[70:73], v[142:145]
	v_mfma_f32_16x16x32_bf16 v[102:105], v[122:125], v[70:73], v[102:105]
	v_mfma_f32_16x16x32_bf16 v[142:145], v[110:113], v[74:77], v[142:145]
	v_mfma_f32_16x16x32_bf16 v[102:105], v[126:129], v[74:77], v[102:105]
	v_mfma_f32_16x16x32_bf16 v[154:157], v[114:117], v[82:85], v[142:145]
	v_mfma_f32_16x16x32_bf16 v[150:153], v[130:133], v[82:85], v[102:105]
	v_mfma_f32_16x16x32_bf16 v[102:105], v[118:121], v[94:97], 0
	s_nop 5
	v_max3_f32 v189, v155, v156, v157
	v_max3_f32 v218, v218, v154, v189
	v_max3_f32 v189, v151, v152, v153
	v_mfma_f32_16x16x32_bf16 v[102:105], v[122:125], v[86:89], v[102:105]
	v_max3_f32 v218, v218, v150, v189
	v_mov_b32_e32 v189, v218
	s_nop 1
	v_permlane16_swap_b32_e32 v218, v189
	v_mfma_f32_16x16x32_bf16 v[102:105], v[126:129], v[90:93], v[102:105]
	v_max_f32 v218, v218, v189
	s_nop 0
	v_mov_b32_e32 v189, v218
	s_nop 1
	v_permlane32_swap_b32_e32 v218, v189
	v_max_f32 v218, v218, v189
	v_mfma_f32_16x16x32_bf16 v[142:145], v[130:133], v[98:101], v[102:105]
	v_mul_f32_e32 v218, 0x3e0293ee, v218
	v_add_f32_e32 v189, 0x41000000, v187
	v_cmp_gt_f32_e32 vcc, v218, v189
	ds_read_b64_tr_b16 v[130:131], v237 offset:49152
	ds_read_b64_tr_b16 v[132:133], v237 offset:53248
	ds_read_b64_tr_b16 v[122:123], v237 offset:57344
	ds_read_b64_tr_b16 v[124:125], v237 offset:61440
	ds_read_b64_tr_b16 v[126:127], v238 offset:49152
	ds_read_b64_tr_b16 v[128:129], v238 offset:53248
	ds_read_b64_tr_b16 v[114:115], v238 offset:57344
	ds_read_b64_tr_b16 v[116:117], v238 offset:61440
	v_cndmask_b32_e32 v218, v187, v218, vcc
	ds_read_b64_tr_b16 v[118:119], v239 offset:49152
	ds_read_b64_tr_b16 v[120:121], v239 offset:53248
	ds_read_b64_tr_b16 v[110:111], v239 offset:57344
	ds_read_b64_tr_b16 v[112:113], v239 offset:61440
	ds_read_b64_tr_b16 v[106:107], v240 offset:49152
	ds_read_b64_tr_b16 v[108:109], v240 offset:53248
	ds_read_b64_tr_b16 v[102:103], v240 offset:57344
	ds_read_b64_tr_b16 v[104:105], v240 offset:61440
	ds_read_b64 v[198:199], v213
	v_fma_f32 v162, v162, s97, -v218
	v_exp_f32_e32 v162, v162
	v_fma_f32 v163, v163, s97, -v218
	v_exp_f32_e32 v163, v163
	v_fma_f32 v164, v164, s97, -v218
	v_exp_f32_e32 v164, v164
	v_fma_f32 v165, v165, s97, -v218
	v_exp_f32_e32 v165, v165
	v_fma_f32 v158, v158, s97, -v218
	s_waitcnt lgkmcnt(0)
	v_lshrrev_b64 v[216:217], v170, v[198:199]
	v_bfe_i32 v198, v216, 0, 1
	v_exp_f32_e32 v158, v158
	v_and_b32_e32 v162, v198, v162
	v_fma_f32 v159, v159, s97, -v218
	v_bfe_i32 v199, v216, 1, 1
	v_and_b32_e32 v163, v199, v163
	v_exp_f32_e32 v159, v159
	v_fma_f32 v160, v160, s97, -v218
	v_add_f32_e32 v198, v162, v163
	v_bfe_i32 v199, v216, 2, 1
	v_exp_f32_e32 v160, v160
	v_and_b32_e32 v164, v199, v164
	v_fma_f32 v161, v161, s97, -v218
	v_bfe_i32 v200, v216, 3, 1
	v_add_f32_e32 v198, v198, v164
	v_and_b32_e32 v165, v200, v165
	v_exp_f32_e32 v161, v161
	v_fma_f32 v154, v154, s97, -v218
	v_add_f32_e32 v198, v198, v165
	v_bfe_i32 v199, v216, 16, 1
	v_exp_f32_e32 v154, v154
	v_and_b32_e32 v158, v199, v158
	v_fma_f32 v155, v155, s97, -v218
	v_bfe_i32 v200, v216, 17, 1
	v_add_f32_e32 v198, v198, v158
	v_and_b32_e32 v159, v200, v159
	v_exp_f32_e32 v155, v155
	v_fma_f32 v156, v156, s97, -v218
	v_add_f32_e32 v198, v198, v159
	v_bfe_i32 v199, v216, 18, 1
	v_exp_f32_e32 v156, v156
	v_and_b32_e32 v160, v199, v160
	v_fma_f32 v157, v157, s97, -v218
	v_bfe_i32 v200, v216, 19, 1
	v_add_f32_e32 v198, v198, v160
	v_and_b32_e32 v161, v200, v161
	v_exp_f32_e32 v157, v157
	v_add_f32_e32 v198, v198, v161
	v_bfe_i32 v199, v217, 0, 1
	v_fma_f32 v150, v150, s97, -v218
	v_and_b32_e32 v154, v199, v154
	v_bfe_i32 v200, v217, 1, 1
	v_add_f32_e32 v198, v198, v154
	v_and_b32_e32 v155, v200, v155
	v_exp_f32_e32 v150, v150
	v_fma_f32 v151, v151, s97, -v218
	v_add_f32_e32 v198, v198, v155
	v_bfe_i32 v199, v217, 2, 1
	v_exp_f32_e32 v151, v151
	v_and_b32_e32 v216, v199, v156
	v_fma_f32 v152, v152, s97, -v218
	v_bfe_i32 v200, v217, 3, 1
	v_add_f32_e32 v156, v198, v216
	v_and_b32_e32 v157, v200, v157
	v_exp_f32_e32 v152, v152
	v_fma_f32 v153, v153, s97, -v218
	v_add_f32_e32 v198, v156, v157
	v_bfe_i32 v156, v217, 16, 1
	v_exp_f32_e32 v153, v153
	v_and_b32_e32 v156, v156, v150
	v_bfe_i32 v199, v217, 17, 1
	v_add_f32_e32 v150, v198, v156
	v_and_b32_e32 v151, v199, v151
	v_add_f32_e32 v150, v150, v151
	v_bfe_i32 v198, v217, 18, 1
	v_sub_f32_e32 v189, v187, v218
	v_and_b32_e32 v152, v198, v152
	v_bfe_i32 v199, v217, 19, 1
	v_add_f32_e32 v150, v150, v152
	v_and_b32_e32 v153, v199, v153
	v_add_f32_e32 v198, v150, v153
	v_exp_f32_e32 v150, v189
	s_nop 0
	v_cmp_eq_f32_e32 vcc, 1.0, v150
	v_fma_f32 v215, v215, v150, v198
	s_cmp_eq_u64 vcc, exec
	s_cbranch_scc1 .Lat0_O_1260
	v_pk_mul_f32 v[68:69], v[68:69], v[150:151] op_sel_hi:[1,0]
	v_pk_mul_f32 v[66:67], v[66:67], v[150:151] op_sel_hi:[1,0]
	v_pk_mul_f32 v[64:65], v[64:65], v[150:151] op_sel_hi:[1,0]
	v_pk_mul_f32 v[62:63], v[62:63], v[150:151] op_sel_hi:[1,0]
	v_pk_mul_f32 v[60:61], v[60:61], v[150:151] op_sel_hi:[1,0]
	v_pk_mul_f32 v[58:59], v[58:59], v[150:151] op_sel_hi:[1,0]
	v_pk_mul_f32 v[56:57], v[56:57], v[150:151] op_sel_hi:[1,0]
	v_pk_mul_f32 v[54:55], v[54:55], v[150:151] op_sel_hi:[1,0]
	v_pk_mul_f32 v[52:53], v[52:53], v[150:151] op_sel_hi:[1,0]
	v_pk_mul_f32 v[50:51], v[50:51], v[150:151] op_sel_hi:[1,0]
	v_pk_mul_f32 v[48:49], v[48:49], v[150:151] op_sel_hi:[1,0]
	v_pk_mul_f32 v[46:47], v[46:47], v[150:151] op_sel_hi:[1,0]
	v_pk_mul_f32 v[44:45], v[44:45], v[150:151] op_sel_hi:[1,0]
	v_pk_mul_f32 v[42:43], v[42:43], v[150:151] op_sel_hi:[1,0]
	v_pk_mul_f32 v[40:41], v[40:41], v[150:151] op_sel_hi:[1,0]
	v_pk_mul_f32 v[38:39], v[38:39], v[150:151] op_sel_hi:[1,0]
.Lat0_O_1260:
	v_max_f32_e32 v200, v136, v137
	v_max3_f32 v200, v134, v135, v200
	v_max3_f32 v201, v139, v140, v141
	v_max3_f32 v200, v200, v138, v201
	v_max3_f32 v201, v147, v148, v149
	v_max3_f32 v200, v200, v146, v201
	v_max3_f32 v201, v143, v144, v145
	v_max3_f32 v200, v200, v142, v201
	v_mov_b32_e32 v201, v200
	s_nop 1
	v_permlane16_swap_b32_e32 v200, v201
	v_max_f32 v200, v200, v201
	ds_read_b64 v[198:199], v213 offset:8192
	v_mov_b32_e32 v201, v200
	s_nop 1
	v_permlane32_swap_b32_e32 v200, v201
	v_max_f32 v200, v200, v201
	v_add_f32_e32 v201, 0x41000000, v249
	v_mul_f32_e32 v200, 0x3e0293ee, v200
	v_cmp_gt_f32_e32 vcc, v200, v201
	s_waitcnt lgkmcnt(0)
	v_lshrrev_b64 v[198:199], v170, v[198:199]
	v_bfe_i32 v201, v198, 0, 1
	v_cndmask_b32_e32 v167, v249, v200, vcc
	v_fma_f32 v135, v135, s97, -v167
	v_exp_f32_e32 v135, v135
	v_sub_f32_e32 v200, v249, v167
	v_bfe_i32 v249, v198, 1, 1
	v_fma_f32 v134, v134, s97, -v167
	v_and_b32_e32 v249, v249, v135
	v_fma_f32 v135, v136, s97, -v167
	v_fma_f32 v136, v137, s97, -v167
	v_exp_f32_e32 v134, v134
	v_exp_f32_e32 v136, v136
	v_exp_f32_e32 v137, v135
	v_bfe_i32 v135, v198, 3, 1
	v_and_b32_e32 v187, v201, v134
	v_bfe_i32 v201, v198, 2, 1
	v_and_b32_e32 v135, v135, v136
	v_and_b32_e32 v136, v201, v137
	v_fma_f32 v137, v138, s97, -v167
	v_fma_f32 v138, v139, s97, -v167
	v_exp_f32_e32 v138, v138
	v_exp_f32_e32 v139, v137
	v_bfe_i32 v137, v198, 17, 1
	v_bfe_i32 v201, v198, 16, 1
	v_and_b32_e32 v137, v137, v138
	v_and_b32_e32 v138, v201, v139
	v_fma_f32 v139, v140, s97, -v167
	v_fma_f32 v140, v141, s97, -v167
	v_exp_f32_e32 v140, v140
	v_exp_f32_e32 v141, v139
	v_bfe_i32 v139, v198, 19, 1
	v_bfe_i32 v201, v198, 18, 1
	v_add_f32_e32 v134, v187, v249
	v_and_b32_e32 v139, v139, v140
	v_and_b32_e32 v140, v201, v141
	v_fma_f32 v141, v146, s97, -v167
	v_fma_f32 v146, v147, s97, -v167
	v_exp_f32_e32 v146, v146
	v_exp_f32_e32 v147, v141
	v_add_f32_e32 v134, v134, v136
	v_add_f32_e32 v134, v134, v135
	v_bfe_i32 v141, v199, 1, 1
	v_add_f32_e32 v134, v134, v138
	v_bfe_i32 v198, v199, 0, 1
	v_and_b32_e32 v141, v141, v146
	v_and_b32_e32 v146, v198, v147
	v_fma_f32 v147, v148, s97, -v167
	v_fma_f32 v148, v149, s97, -v167
	v_add_f32_e32 v134, v134, v137
	v_exp_f32_e32 v148, v148
	v_exp_f32_e32 v149, v147
	v_add_f32_e32 v134, v134, v140
	v_fma_f32 v142, v142, s97, -v167
	v_add_f32_e32 v134, v134, v139
	v_fma_f32 v143, v143, s97, -v167
	v_exp_f32_e32 v142, v142
	v_add_f32_e32 v134, v134, v146
	v_bfe_i32 v147, v199, 3, 1
	v_exp_f32_e32 v143, v143
	v_fma_f32 v144, v144, s97, -v167
	v_add_f32_e32 v134, v134, v141
	v_bfe_i32 v198, v199, 2, 1
	v_and_b32_e32 v147, v147, v148
	v_and_b32_e32 v148, v198, v149
	v_fma_f32 v145, v145, s97, -v167
	v_exp_f32_e32 v144, v144
	v_add_f32_e32 v134, v134, v148
	v_exp_f32_e32 v145, v145
	v_add_f32_e32 v134, v134, v147
	v_bfe_i32 v149, v199, 16, 1
	v_bfe_i32 v198, v199, 17, 1
	s_nop 0
	v_and_b32_e32 v142, v149, v142
	v_and_b32_e32 v143, v198, v143
	v_add_f32_e32 v134, v134, v142
	v_add_f32_e32 v134, v134, v143
	v_bfe_i32 v149, v199, 18, 1
	v_bfe_i32 v198, v199, 19, 1
	s_nop 0
	v_and_b32_e32 v144, v149, v144
	v_and_b32_e32 v145, v198, v145
	v_add_f32_e32 v134, v134, v144
	v_add_f32_e32 v149, v134, v145
	v_exp_f32_e32 v134, v200
	s_nop 0
	v_cmp_eq_f32_e32 vcc, 1.0, v134
	v_fma_f32 v248, v248, v134, v149
	s_cmp_eq_u64 vcc, exec
	s_cbranch_scc1 .Lat0_O_1262
	v_pk_mul_f32 v[30:31], v[30:31], v[134:135] op_sel_hi:[1,0]
	v_pk_mul_f32 v[28:29], v[28:29], v[134:135] op_sel_hi:[1,0]
	v_pk_mul_f32 v[26:27], v[26:27], v[134:135] op_sel_hi:[1,0]
	v_pk_mul_f32 v[24:25], v[24:25], v[134:135] op_sel_hi:[1,0]
	v_pk_mul_f32 v[22:23], v[22:23], v[134:135] op_sel_hi:[1,0]
	v_pk_mul_f32 v[20:21], v[20:21], v[134:135] op_sel_hi:[1,0]
	v_pk_mul_f32 v[18:19], v[18:19], v[134:135] op_sel_hi:[1,0]
	v_pk_mul_f32 v[16:17], v[16:17], v[134:135] op_sel_hi:[1,0]
	v_pk_mul_f32 v[14:15], v[14:15], v[134:135] op_sel_hi:[1,0]
	v_pk_mul_f32 v[12:13], v[12:13], v[134:135] op_sel_hi:[1,0]
	v_pk_mul_f32 v[10:11], v[10:11], v[134:135] op_sel_hi:[1,0]
	v_pk_mul_f32 v[8:9], v[8:9], v[134:135] op_sel_hi:[1,0]
	v_pk_mul_f32 v[6:7], v[6:7], v[134:135] op_sel_hi:[1,0]
	v_pk_mul_f32 v[4:5], v[4:5], v[134:135] op_sel_hi:[1,0]
	v_pk_mul_f32 v[2:3], v[2:3], v[134:135] op_sel_hi:[1,0]
	v_pk_mul_f32 v[0:1], v[0:1], v[134:135] op_sel_hi:[1,0]
.Lat0_O_1262:
	v_cvt_pk_bf16_f32 v162, v162, v163
	v_cvt_pk_bf16_f32 v163, v164, v165
	v_cvt_pk_bf16_f32 v164, v158, v159
	v_cvt_pk_bf16_f32 v165, v160, v161
	v_cvt_pk_bf16_f32 v158, v187, v249
	v_cvt_pk_bf16_f32 v159, v136, v135
	v_cvt_pk_bf16_f32 v160, v138, v137
	v_cvt_pk_bf16_f32 v161, v140, v139
	v_mfma_f32_16x16x32_bf16 v[54:57], v[106:109], v[162:165], v[54:57]
	v_cvt_pk_bf16_f32 v154, v154, v155
	v_cvt_pk_bf16_f32 v155, v216, v157
	v_cvt_pk_bf16_f32 v156, v156, v151
	v_mfma_f32_16x16x32_bf16 v[16:19], v[106:109], v[158:161], v[16:19]
	v_cvt_pk_bf16_f32 v157, v152, v153
	s_add_i32 s31, s31, 1
	v_mfma_f32_16x16x32_bf16 v[66:69], v[130:133], v[162:165], v[66:69]
	v_add_u32_e32 v213, 8, v213
	s_cmp_eq_u32 s30, s31
	v_mfma_f32_16x16x32_bf16 v[28:31], v[130:133], v[158:161], v[28:31]
	v_cvt_pk_bf16_f32 v130, v146, v141
	v_cvt_pk_bf16_f32 v131, v148, v147
	v_cvt_pk_bf16_f32 v132, v142, v143
	v_cvt_pk_bf16_f32 v133, v144, v145
	v_mfma_f32_16x16x32_bf16 v[54:57], v[102:105], v[154:157], v[54:57]
	s_nop 0
	v_mfma_f32_16x16x32_bf16 v[16:19], v[102:105], v[130:133], v[16:19]
	ds_read_b64_tr_b16 v[102:103], v241 offset:49152
	ds_read_b64_tr_b16 v[104:105], v241 offset:53248
	ds_read_b64_tr_b16 v[106:107], v241 offset:57344
	ds_read_b64_tr_b16 v[108:109], v241 offset:61440
	v_mfma_f32_16x16x32_bf16 v[58:61], v[118:121], v[162:165], v[58:61]
	v_mfma_f32_16x16x32_bf16 v[20:23], v[118:121], v[158:161], v[20:23]
	s_waitcnt lgkmcnt(2)
	v_mfma_f32_16x16x32_bf16 v[50:53], v[102:105], v[162:165], v[50:53]
	v_mfma_f32_16x16x32_bf16 v[12:15], v[102:105], v[158:161], v[12:15]
	v_mfma_f32_16x16x32_bf16 v[58:61], v[110:113], v[154:157], v[58:61]
	v_mfma_f32_16x16x32_bf16 v[20:23], v[110:113], v[130:133], v[20:23]
	s_waitcnt lgkmcnt(0)
	v_mfma_f32_16x16x32_bf16 v[50:53], v[106:109], v[154:157], v[50:53]
	v_mfma_f32_16x16x32_bf16 v[12:15], v[106:109], v[130:133], v[12:15]
	ds_read_b64_tr_b16 v[102:103], v242 offset:49152
	ds_read_b64_tr_b16 v[104:105], v242 offset:53248
	ds_read_b64_tr_b16 v[106:107], v242 offset:57344
	ds_read_b64_tr_b16 v[108:109], v242 offset:61440
	s_waitcnt lgkmcnt(2)
	v_mfma_f32_16x16x32_bf16 v[46:49], v[102:105], v[162:165], v[46:49]
	v_mfma_f32_16x16x32_bf16 v[8:11], v[102:105], v[158:161], v[8:11]
	s_waitcnt lgkmcnt(0)
	v_mfma_f32_16x16x32_bf16 v[46:49], v[106:109], v[154:157], v[46:49]
	v_mfma_f32_16x16x32_bf16 v[8:11], v[106:109], v[130:133], v[8:11]
	ds_read_b64_tr_b16 v[102:103], v243 offset:49152
	ds_read_b64_tr_b16 v[104:105], v243 offset:53248
	ds_read_b64_tr_b16 v[106:107], v243 offset:57344
	ds_read_b64_tr_b16 v[108:109], v243 offset:61440
	s_waitcnt lgkmcnt(2)
	v_mfma_f32_16x16x32_bf16 v[42:45], v[102:105], v[162:165], v[42:45]
	v_mfma_f32_16x16x32_bf16 v[4:7], v[102:105], v[158:161], v[4:7]
	ds_read_b64_tr_b16 v[110:111], v244 offset:49152
	ds_read_b64_tr_b16 v[112:113], v244 offset:53248
	s_waitcnt lgkmcnt(2)
	v_mfma_f32_16x16x32_bf16 v[42:45], v[106:109], v[154:157], v[42:45]
	v_mfma_f32_16x16x32_bf16 v[4:7], v[106:109], v[130:133], v[4:7]
	ds_read_b64_tr_b16 v[104:105], v244 offset:57344
	ds_read_b64_tr_b16 v[106:107], v244 offset:61440
	s_waitcnt vmcnt(0)
	v_mfma_f32_16x16x32_bf16 v[62:65], v[126:129], v[162:165], v[62:65]
	s_waitcnt lgkmcnt(0)
	s_barrier
	v_mfma_f32_16x16x32_bf16 v[24:27], v[126:129], v[158:161], v[24:27]
	v_mfma_f32_16x16x32_bf16 v[38:41], v[110:113], v[162:165], v[38:41]
	v_mfma_f32_16x16x32_bf16 v[0:3], v[110:113], v[158:161], v[0:3]
	v_mfma_f32_16x16x32_bf16 v[66:69], v[122:125], v[154:157], v[66:69]
	v_mfma_f32_16x16x32_bf16 v[28:31], v[122:125], v[130:133], v[28:31]
	v_mfma_f32_16x16x32_bf16 v[62:65], v[114:117], v[154:157], v[62:65]
	v_mfma_f32_16x16x32_bf16 v[24:27], v[114:117], v[130:133], v[24:27]
	v_mfma_f32_16x16x32_bf16 v[38:41], v[104:107], v[154:157], v[38:41]
	v_mfma_f32_16x16x32_bf16 v[0:3], v[104:107], v[130:133], v[0:3]
	s_cbranch_scc0 .LBB0_1254
	v_mov_b32_e32 v189, v215
	v_mov_b32_e32 v198, v248
	s_nop 1
	v_permlane16_swap_b32_e32 v215, v189
	v_permlane16_swap_b32_e32 v248, v198
	v_add_f32_e32 v189, v215, v189
	v_add_f32_e32 v198, v248, v198
	v_mov_b32_e32 v217, v189
	v_mov_b32_e32 v250, v198
	s_nop 1
	v_permlane32_swap_b32_e32 v189, v217
	v_permlane32_swap_b32_e32 v198, v250
	v_add_f32_e32 v103, v189, v217
	v_add_f32_e32 v102, v198, v250
	s_branch .LBB0_1251

.LBB0_1283:
	s_and_b32 s20, s18, 1
	s_cmp_lt_i32 s18, s16
	s_mov_b64 s[8:9], -1
	s_cbranch_scc1 .LBB0_1285

.Lat16_O_1287:
	ds_read_b128 v[102:105], v171 offset:16384
	ds_read_b128 v[106:109], v219 offset:16384
	ds_read_b128 v[110:113], v222 offset:16384
	ds_read_b128 v[114:117], v223 offset:16384
	ds_read_b128 v[118:121], v171 offset:20480
	ds_read_b128 v[122:125], v219 offset:20480
	ds_read_b128 v[126:129], v222 offset:20480
	ds_read_b128 v[130:133], v223 offset:20480
	s_waitcnt lgkmcnt(0)
	v_mfma_f32_16x16x32_bf16 v[138:141], v[118:121], v[78:81], 0
	v_mfma_f32_16x16x32_bf16 v[134:137], v[102:105], v[78:81], 0
	v_mfma_f32_16x16x32_bf16 v[102:105], v[102:105], v[94:97], 0
	v_mfma_f32_16x16x32_bf16 v[118:121], v[118:121], v[94:97], 0
	v_mfma_f32_16x16x32_bf16 v[134:137], v[106:109], v[70:73], v[134:137]
	v_mfma_f32_16x16x32_bf16 v[102:105], v[106:109], v[86:89], v[102:105]
	v_mfma_f32_16x16x32_bf16 v[138:141], v[122:125], v[70:73], v[138:141]
	v_mfma_f32_16x16x32_bf16 v[118:121], v[122:125], v[86:89], v[118:121]
	v_mfma_f32_16x16x32_bf16 v[134:137], v[110:113], v[74:77], v[134:137]
	v_mfma_f32_16x16x32_bf16 v[102:105], v[110:113], v[90:93], v[102:105]
	v_mfma_f32_16x16x32_bf16 v[138:141], v[126:129], v[74:77], v[138:141]
	v_mfma_f32_16x16x32_bf16 v[118:121], v[126:129], v[90:93], v[118:121]
	v_mfma_f32_16x16x32_bf16 v[162:165], v[114:117], v[82:85], v[134:137]
	v_mfma_f32_16x16x32_bf16 v[134:137], v[114:117], v[98:101], v[102:105]
	s_nop 3
	ds_read_b128 v[102:105], v171 offset:24576
	ds_read_b128 v[106:109], v219 offset:24576
	ds_read_b128 v[110:113], v222 offset:24576
	ds_read_b128 v[114:117], v223 offset:24576
	v_max_f32_e32 v167, v164, v165
	v_mfma_f32_16x16x32_bf16 v[158:161], v[130:133], v[82:85], v[138:141]
	v_max3_f32 v167, v162, v163, v167
	v_mfma_f32_16x16x32_bf16 v[138:141], v[130:133], v[98:101], v[118:121]
	s_nop 2
	ds_read_b128 v[118:121], v171 offset:28672
	ds_read_b128 v[122:125], v219 offset:28672
	ds_read_b128 v[126:129], v222 offset:28672
	ds_read_b128 v[130:133], v223 offset:28672
	v_max3_f32 v246, v159, v160, v161
	v_max3_f32 v167, v167, v158, v246
	s_waitcnt lgkmcnt(0)
	v_mfma_f32_16x16x32_bf16 v[142:145], v[102:105], v[78:81], 0
	v_mfma_f32_16x16x32_bf16 v[102:105], v[102:105], v[94:97], 0
	v_mfma_f32_16x16x32_bf16 v[102:105], v[106:109], v[86:89], v[102:105]
	v_mfma_f32_16x16x32_bf16 v[102:105], v[110:113], v[90:93], v[102:105]
	v_mfma_f32_16x16x32_bf16 v[146:149], v[114:117], v[98:101], v[102:105]
	v_mfma_f32_16x16x32_bf16 v[102:105], v[118:121], v[78:81], 0
	v_mfma_f32_16x16x32_bf16 v[142:145], v[106:109], v[70:73], v[142:145]
	v_mfma_f32_16x16x32_bf16 v[102:105], v[122:125], v[70:73], v[102:105]
	v_mfma_f32_16x16x32_bf16 v[142:145], v[110:113], v[74:77], v[142:145]
	v_mfma_f32_16x16x32_bf16 v[102:105], v[126:129], v[74:77], v[102:105]
	v_mfma_f32_16x16x32_bf16 v[154:157], v[114:117], v[82:85], v[142:145]
	v_mfma_f32_16x16x32_bf16 v[150:153], v[130:133], v[82:85], v[102:105]
	v_mfma_f32_16x16x32_bf16 v[102:105], v[118:121], v[94:97], 0
	s_nop 5
	v_max3_f32 v246, v155, v156, v157
	v_max3_f32 v167, v167, v154, v246
	v_max3_f32 v246, v151, v152, v153
	v_mfma_f32_16x16x32_bf16 v[102:105], v[122:125], v[86:89], v[102:105]
	v_max3_f32 v167, v167, v150, v246
	v_mov_b32_e32 v246, v167
	s_nop 1
	v_permlane16_swap_b32_e32 v167, v246
	v_mfma_f32_16x16x32_bf16 v[102:105], v[126:129], v[90:93], v[102:105]
	v_max_f32 v167, v167, v246
	s_nop 0
	v_mov_b32_e32 v246, v167
	s_nop 1
	v_permlane32_swap_b32_e32 v167, v246
	v_max_f32 v167, v167, v246
	v_mfma_f32_16x16x32_bf16 v[142:145], v[130:133], v[98:101], v[102:105]
	v_mul_f32_e32 v167, 0x3e0293ee, v167
	v_add_f32_e32 v246, 0x41000000, v189
	v_cmp_gt_f32_e32 vcc, v167, v246
	ds_read_b64_tr_b16 v[130:131], v224 offset:49152
	ds_read_b64_tr_b16 v[132:133], v224 offset:53248
	ds_read_b64_tr_b16 v[122:123], v224 offset:57344
	ds_read_b64_tr_b16 v[124:125], v224 offset:61440
	ds_read_b64_tr_b16 v[126:127], v225 offset:49152
	ds_read_b64_tr_b16 v[128:129], v225 offset:53248
	ds_read_b64_tr_b16 v[114:115], v225 offset:57344
	ds_read_b64_tr_b16 v[116:117], v225 offset:61440
	v_cndmask_b32_e32 v246, v189, v167, vcc
	ds_read_b64_tr_b16 v[118:119], v237 offset:49152
	ds_read_b64_tr_b16 v[120:121], v237 offset:53248
	ds_read_b64_tr_b16 v[110:111], v237 offset:57344
	ds_read_b64_tr_b16 v[112:113], v237 offset:61440
	ds_read_b64_tr_b16 v[106:107], v238 offset:49152
	ds_read_b64_tr_b16 v[108:109], v238 offset:53248
	ds_read_b64_tr_b16 v[102:103], v238 offset:57344
	ds_read_b64_tr_b16 v[104:105], v238 offset:61440
	ds_read_b64 v[198:199], v213
	v_fma_f32 v162, v162, s97, -v246
	v_exp_f32_e32 v162, v162
	v_fma_f32 v163, v163, s97, -v246
	v_exp_f32_e32 v163, v163
	v_fma_f32 v164, v164, s97, -v246
	v_exp_f32_e32 v164, v164
	v_fma_f32 v165, v165, s97, -v246
	v_exp_f32_e32 v165, v165
	v_fma_f32 v158, v158, s97, -v246
	s_waitcnt lgkmcnt(0)
	v_lshrrev_b64 v[216:217], v170, v[198:199]
	v_bfe_i32 v198, v216, 0, 1
	v_exp_f32_e32 v158, v158
	v_and_b32_e32 v162, v198, v162
	v_fma_f32 v159, v159, s97, -v246
	v_bfe_i32 v199, v216, 1, 1
	v_and_b32_e32 v163, v199, v163
	v_exp_f32_e32 v159, v159
	v_fma_f32 v160, v160, s97, -v246
	v_add_f32_e32 v198, v162, v163
	v_bfe_i32 v199, v216, 2, 1
	v_exp_f32_e32 v160, v160
	v_and_b32_e32 v164, v199, v164
	v_fma_f32 v161, v161, s97, -v246
	v_bfe_i32 v200, v216, 3, 1
	v_add_f32_e32 v198, v198, v164
	v_and_b32_e32 v165, v200, v165
	v_exp_f32_e32 v161, v161
	v_fma_f32 v154, v154, s97, -v246
	v_add_f32_e32 v198, v198, v165
	v_bfe_i32 v199, v216, 16, 1
	v_exp_f32_e32 v154, v154
	v_and_b32_e32 v158, v199, v158
	v_fma_f32 v155, v155, s97, -v246
	v_bfe_i32 v200, v216, 17, 1
	v_add_f32_e32 v198, v198, v158
	v_and_b32_e32 v159, v200, v159
	v_exp_f32_e32 v155, v155
	v_fma_f32 v156, v156, s97, -v246
	v_add_f32_e32 v198, v198, v159
	v_bfe_i32 v199, v216, 18, 1
	v_exp_f32_e32 v156, v156
	v_and_b32_e32 v160, v199, v160
	v_fma_f32 v157, v157, s97, -v246
	v_bfe_i32 v200, v216, 19, 1
	v_add_f32_e32 v198, v198, v160
	v_and_b32_e32 v161, v200, v161
	v_exp_f32_e32 v157, v157
	v_add_f32_e32 v198, v198, v161
	v_bfe_i32 v199, v217, 0, 1
	v_fma_f32 v150, v150, s97, -v246
	v_and_b32_e32 v154, v199, v154
	v_bfe_i32 v200, v217, 1, 1
	v_add_f32_e32 v198, v198, v154
	v_and_b32_e32 v155, v200, v155
	v_exp_f32_e32 v150, v150
	v_fma_f32 v151, v151, s97, -v246
	v_add_f32_e32 v198, v198, v155
	v_bfe_i32 v199, v217, 2, 1
	v_exp_f32_e32 v151, v151
	v_and_b32_e32 v216, v199, v156
	v_fma_f32 v152, v152, s97, -v246
	v_bfe_i32 v200, v217, 3, 1
	v_add_f32_e32 v156, v198, v216
	v_and_b32_e32 v157, v200, v157
	v_exp_f32_e32 v152, v152
	v_fma_f32 v153, v153, s97, -v246
	v_add_f32_e32 v198, v156, v157
	v_bfe_i32 v156, v217, 16, 1
	v_exp_f32_e32 v153, v153
	v_and_b32_e32 v156, v156, v150
	v_bfe_i32 v199, v217, 17, 1
	v_add_f32_e32 v150, v198, v156
	v_and_b32_e32 v151, v199, v151
	v_add_f32_e32 v150, v150, v151
	v_bfe_i32 v198, v217, 18, 1
	v_sub_f32_e32 v167, v189, v246
	v_and_b32_e32 v152, v198, v152
	v_bfe_i32 v199, v217, 19, 1
	v_add_f32_e32 v150, v150, v152
	v_and_b32_e32 v153, v199, v153
	v_add_f32_e32 v198, v150, v153
	v_exp_f32_e32 v150, v167
	s_nop 0
	v_cmp_eq_f32_e32 vcc, 1.0, v150
	v_fma_f32 v215, v215, v150, v198
	s_cmp_eq_u64 vcc, exec
	s_cbranch_scc1 .Lat16_O_1289
	v_pk_mul_f32 v[68:69], v[68:69], v[150:151] op_sel_hi:[1,0]
	v_pk_mul_f32 v[66:67], v[66:67], v[150:151] op_sel_hi:[1,0]
	v_pk_mul_f32 v[64:65], v[64:65], v[150:151] op_sel_hi:[1,0]
	v_pk_mul_f32 v[62:63], v[62:63], v[150:151] op_sel_hi:[1,0]
	v_pk_mul_f32 v[60:61], v[60:61], v[150:151] op_sel_hi:[1,0]
	v_pk_mul_f32 v[58:59], v[58:59], v[150:151] op_sel_hi:[1,0]
	v_pk_mul_f32 v[56:57], v[56:57], v[150:151] op_sel_hi:[1,0]
	v_pk_mul_f32 v[54:55], v[54:55], v[150:151] op_sel_hi:[1,0]
	v_pk_mul_f32 v[52:53], v[52:53], v[150:151] op_sel_hi:[1,0]
	v_pk_mul_f32 v[50:51], v[50:51], v[150:151] op_sel_hi:[1,0]
	v_pk_mul_f32 v[48:49], v[48:49], v[150:151] op_sel_hi:[1,0]
	v_pk_mul_f32 v[46:47], v[46:47], v[150:151] op_sel_hi:[1,0]
	v_pk_mul_f32 v[40:41], v[40:41], v[150:151] op_sel_hi:[1,0]
	v_pk_mul_f32 v[38:39], v[38:39], v[150:151] op_sel_hi:[1,0]
	v_pk_mul_f32 v[44:45], v[44:45], v[150:151] op_sel_hi:[1,0]
	v_pk_mul_f32 v[42:43], v[42:43], v[150:151] op_sel_hi:[1,0]
.Lat16_O_1289:
	v_max_f32_e32 v167, v136, v137
	v_max3_f32 v167, v134, v135, v167
	v_max3_f32 v200, v139, v140, v141
	v_max3_f32 v167, v167, v138, v200
	v_max3_f32 v200, v147, v148, v149
	v_max3_f32 v167, v167, v146, v200
	v_max3_f32 v200, v143, v144, v145
	v_max3_f32 v167, v167, v142, v200
	v_mov_b32_e32 v200, v167
	s_nop 1
	v_permlane16_swap_b32_e32 v167, v200
	v_max_f32 v167, v167, v200
	ds_read_b64 v[198:199], v213 offset:8192
	v_mov_b32_e32 v200, v167
	s_nop 1
	v_permlane32_swap_b32_e32 v167, v200
	v_max_f32 v167, v167, v200
	v_add_f32_e32 v200, 0x41000000, v247
	v_mul_f32_e32 v167, 0x3e0293ee, v167
	v_cmp_gt_f32_e32 vcc, v167, v200
	s_waitcnt lgkmcnt(0)
	v_lshrrev_b64 v[198:199], v170, v[198:199]
	v_bfe_i32 v201, v198, 0, 1
	v_cndmask_b32_e32 v218, v247, v167, vcc
	v_fma_f32 v135, v135, s97, -v218
	v_exp_f32_e32 v135, v135
	v_bfe_i32 v167, v198, 1, 1
	v_fma_f32 v134, v134, s97, -v218
	v_exp_f32_e32 v134, v134
	v_and_b32_e32 v167, v167, v135
	v_fma_f32 v135, v136, s97, -v218
	v_fma_f32 v136, v137, s97, -v218
	v_exp_f32_e32 v136, v136
	v_exp_f32_e32 v137, v135
	v_bfe_i32 v135, v198, 3, 1
	v_sub_f32_e32 v200, v247, v218
	v_and_b32_e32 v247, v201, v134
	v_bfe_i32 v201, v198, 2, 1
	v_and_b32_e32 v135, v135, v136
	v_and_b32_e32 v136, v201, v137
	v_fma_f32 v137, v138, s97, -v218
	v_fma_f32 v138, v139, s97, -v218
	v_exp_f32_e32 v138, v138
	v_exp_f32_e32 v139, v137
	v_bfe_i32 v137, v198, 17, 1
	v_bfe_i32 v201, v198, 16, 1
	v_and_b32_e32 v137, v137, v138
	v_and_b32_e32 v138, v201, v139
	v_fma_f32 v139, v140, s97, -v218
	v_fma_f32 v140, v141, s97, -v218
	v_exp_f32_e32 v140, v140
	v_exp_f32_e32 v141, v139
	v_bfe_i32 v139, v198, 19, 1
	v_bfe_i32 v201, v198, 18, 1
	v_add_f32_e32 v134, v247, v167
	v_and_b32_e32 v139, v139, v140
	v_and_b32_e32 v140, v201, v141
	v_fma_f32 v141, v146, s97, -v218
	v_fma_f32 v146, v147, s97, -v218
	v_exp_f32_e32 v146, v146
	v_exp_f32_e32 v147, v141
	v_add_f32_e32 v134, v134, v136
	v_add_f32_e32 v134, v134, v135
	v_bfe_i32 v141, v199, 1, 1
	v_add_f32_e32 v134, v134, v138
	v_bfe_i32 v198, v199, 0, 1
	v_and_b32_e32 v141, v141, v146
	v_and_b32_e32 v146, v198, v147
	v_fma_f32 v147, v148, s97, -v218
	v_fma_f32 v148, v149, s97, -v218
	v_add_f32_e32 v134, v134, v137
	v_exp_f32_e32 v148, v148
	v_exp_f32_e32 v149, v147
	v_add_f32_e32 v134, v134, v140
	v_fma_f32 v142, v142, s97, -v218
	v_add_f32_e32 v134, v134, v139
	v_fma_f32 v143, v143, s97, -v218
	v_exp_f32_e32 v142, v142
	v_add_f32_e32 v134, v134, v146
	v_bfe_i32 v147, v199, 3, 1
	v_exp_f32_e32 v143, v143
	v_fma_f32 v144, v144, s97, -v218
	v_add_f32_e32 v134, v134, v141
	v_bfe_i32 v198, v199, 2, 1
	v_and_b32_e32 v147, v147, v148
	v_and_b32_e32 v148, v198, v149
	v_fma_f32 v145, v145, s97, -v218
	v_exp_f32_e32 v144, v144
	v_add_f32_e32 v134, v134, v148
	v_exp_f32_e32 v145, v145
	v_add_f32_e32 v134, v134, v147
	v_bfe_i32 v149, v199, 16, 1
	v_bfe_i32 v198, v199, 17, 1
	s_nop 0
	v_and_b32_e32 v142, v149, v142
	v_and_b32_e32 v143, v198, v143
	v_add_f32_e32 v134, v134, v142
	v_add_f32_e32 v134, v134, v143
	v_bfe_i32 v149, v199, 18, 1
	v_bfe_i32 v198, v199, 19, 1
	s_nop 0
	v_and_b32_e32 v144, v149, v144
	v_and_b32_e32 v145, v198, v145
	v_add_f32_e32 v134, v134, v144
	v_add_f32_e32 v149, v134, v145
	v_exp_f32_e32 v134, v200
	s_nop 0
	v_cmp_eq_f32_e32 vcc, 1.0, v134
	v_fma_f32 v245, v245, v134, v149
	s_cmp_eq_u64 vcc, exec
	s_cbranch_scc1 .Lat16_O_1291
	v_pk_mul_f32 v[30:31], v[30:31], v[134:135] op_sel_hi:[1,0]
	v_pk_mul_f32 v[28:29], v[28:29], v[134:135] op_sel_hi:[1,0]
	v_pk_mul_f32 v[26:27], v[26:27], v[134:135] op_sel_hi:[1,0]
	v_pk_mul_f32 v[24:25], v[24:25], v[134:135] op_sel_hi:[1,0]
	v_pk_mul_f32 v[22:23], v[22:23], v[134:135] op_sel_hi:[1,0]
	v_pk_mul_f32 v[20:21], v[20:21], v[134:135] op_sel_hi:[1,0]
	v_pk_mul_f32 v[18:19], v[18:19], v[134:135] op_sel_hi:[1,0]
	v_pk_mul_f32 v[16:17], v[16:17], v[134:135] op_sel_hi:[1,0]
	v_pk_mul_f32 v[14:15], v[14:15], v[134:135] op_sel_hi:[1,0]
	v_pk_mul_f32 v[12:13], v[12:13], v[134:135] op_sel_hi:[1,0]
	v_pk_mul_f32 v[10:11], v[10:11], v[134:135] op_sel_hi:[1,0]
	v_pk_mul_f32 v[8:9], v[8:9], v[134:135] op_sel_hi:[1,0]
	v_pk_mul_f32 v[6:7], v[6:7], v[134:135] op_sel_hi:[1,0]
	v_pk_mul_f32 v[4:5], v[4:5], v[134:135] op_sel_hi:[1,0]
	v_pk_mul_f32 v[2:3], v[2:3], v[134:135] op_sel_hi:[1,0]
	v_pk_mul_f32 v[0:1], v[0:1], v[134:135] op_sel_hi:[1,0]
.Lat16_O_1291:
	v_cvt_pk_bf16_f32 v162, v162, v163
	v_cvt_pk_bf16_f32 v163, v164, v165
	v_cvt_pk_bf16_f32 v164, v158, v159
	v_cvt_pk_bf16_f32 v165, v160, v161
	v_cvt_pk_bf16_f32 v158, v247, v167
	v_cvt_pk_bf16_f32 v159, v136, v135
	v_cvt_pk_bf16_f32 v160, v138, v137
	v_cvt_pk_bf16_f32 v161, v140, v139
	v_mfma_f32_16x16x32_bf16 v[54:57], v[106:109], v[162:165], v[54:57]
	v_cvt_pk_bf16_f32 v154, v154, v155
	v_cvt_pk_bf16_f32 v155, v216, v157
	v_cvt_pk_bf16_f32 v156, v156, v151
	v_mfma_f32_16x16x32_bf16 v[16:19], v[106:109], v[158:161], v[16:19]
	v_cvt_pk_bf16_f32 v157, v152, v153
	s_add_i32 s18, s18, 1
	v_mfma_f32_16x16x32_bf16 v[66:69], v[130:133], v[162:165], v[66:69]
	v_add_u32_e32 v213, 8, v213
	s_cmp_eq_u32 s17, s18
	v_mfma_f32_16x16x32_bf16 v[28:31], v[130:133], v[158:161], v[28:31]
	v_cvt_pk_bf16_f32 v130, v146, v141
	v_cvt_pk_bf16_f32 v131, v148, v147
	v_cvt_pk_bf16_f32 v132, v142, v143
	v_cvt_pk_bf16_f32 v133, v144, v145
	v_mfma_f32_16x16x32_bf16 v[54:57], v[102:105], v[154:157], v[54:57]
	s_nop 0
	v_mfma_f32_16x16x32_bf16 v[16:19], v[102:105], v[130:133], v[16:19]
	ds_read_b64_tr_b16 v[102:103], v239 offset:49152
	ds_read_b64_tr_b16 v[104:105], v239 offset:53248
	ds_read_b64_tr_b16 v[106:107], v239 offset:57344
	ds_read_b64_tr_b16 v[108:109], v239 offset:61440
	v_mfma_f32_16x16x32_bf16 v[58:61], v[118:121], v[162:165], v[58:61]
	v_mfma_f32_16x16x32_bf16 v[20:23], v[118:121], v[158:161], v[20:23]
	s_waitcnt lgkmcnt(2)
	v_mfma_f32_16x16x32_bf16 v[50:53], v[102:105], v[162:165], v[50:53]
	v_mfma_f32_16x16x32_bf16 v[12:15], v[102:105], v[158:161], v[12:15]
	v_mfma_f32_16x16x32_bf16 v[58:61], v[110:113], v[154:157], v[58:61]
	v_mfma_f32_16x16x32_bf16 v[20:23], v[110:113], v[130:133], v[20:23]
	s_waitcnt lgkmcnt(0)
	v_mfma_f32_16x16x32_bf16 v[50:53], v[106:109], v[154:157], v[50:53]
	v_mfma_f32_16x16x32_bf16 v[12:15], v[106:109], v[130:133], v[12:15]
	ds_read_b64_tr_b16 v[102:103], v240 offset:49152
	ds_read_b64_tr_b16 v[104:105], v240 offset:53248
	ds_read_b64_tr_b16 v[106:107], v240 offset:57344
	ds_read_b64_tr_b16 v[108:109], v240 offset:61440
	s_waitcnt lgkmcnt(2)
	v_mfma_f32_16x16x32_bf16 v[46:49], v[102:105], v[162:165], v[46:49]
	v_mfma_f32_16x16x32_bf16 v[8:11], v[102:105], v[158:161], v[8:11]
	s_waitcnt lgkmcnt(0)
	v_mfma_f32_16x16x32_bf16 v[46:49], v[106:109], v[154:157], v[46:49]
	v_mfma_f32_16x16x32_bf16 v[8:11], v[106:109], v[130:133], v[8:11]
	ds_read_b64_tr_b16 v[102:103], v241 offset:49152
	ds_read_b64_tr_b16 v[104:105], v241 offset:53248
	ds_read_b64_tr_b16 v[106:107], v241 offset:57344
	ds_read_b64_tr_b16 v[108:109], v241 offset:61440
	s_waitcnt lgkmcnt(2)
	v_mfma_f32_16x16x32_bf16 v[38:41], v[102:105], v[162:165], v[38:41]
	v_mfma_f32_16x16x32_bf16 v[4:7], v[102:105], v[158:161], v[4:7]
	ds_read_b64_tr_b16 v[110:111], v242 offset:49152
	ds_read_b64_tr_b16 v[112:113], v242 offset:53248
	s_waitcnt lgkmcnt(2)
	v_mfma_f32_16x16x32_bf16 v[38:41], v[106:109], v[154:157], v[38:41]
	v_mfma_f32_16x16x32_bf16 v[4:7], v[106:109], v[130:133], v[4:7]
	ds_read_b64_tr_b16 v[104:105], v242 offset:57344
	ds_read_b64_tr_b16 v[106:107], v242 offset:61440
	s_waitcnt vmcnt(0)
	v_mfma_f32_16x16x32_bf16 v[62:65], v[126:129], v[162:165], v[62:65]
	s_waitcnt lgkmcnt(0)
	s_barrier
	v_mfma_f32_16x16x32_bf16 v[24:27], v[126:129], v[158:161], v[24:27]
	v_mfma_f32_16x16x32_bf16 v[42:45], v[110:113], v[162:165], v[42:45]
	v_mfma_f32_16x16x32_bf16 v[0:3], v[110:113], v[158:161], v[0:3]
	v_mfma_f32_16x16x32_bf16 v[66:69], v[122:125], v[154:157], v[66:69]
	v_mfma_f32_16x16x32_bf16 v[28:31], v[122:125], v[130:133], v[28:31]
	v_mfma_f32_16x16x32_bf16 v[62:65], v[114:117], v[154:157], v[62:65]
	v_mfma_f32_16x16x32_bf16 v[24:27], v[114:117], v[130:133], v[24:27]
	v_mfma_f32_16x16x32_bf16 v[42:45], v[104:107], v[154:157], v[42:45]
	v_mfma_f32_16x16x32_bf16 v[0:3], v[104:107], v[130:133], v[0:3]
	s_cbranch_scc0 .LBB0_1283
	v_mov_b32_e32 v167, v215
	v_mov_b32_e32 v198, v245
	s_nop 1
	v_permlane16_swap_b32_e32 v215, v167
	v_permlane16_swap_b32_e32 v245, v198
	v_add_f32_e32 v167, v215, v167
	v_add_f32_e32 v198, v245, v198
	v_mov_b32_e32 v217, v167
	v_mov_b32_e32 v248, v198
	s_nop 1
	v_permlane32_swap_b32_e32 v167, v217
	v_permlane32_swap_b32_e32 v198, v248
	v_add_f32_e32 v103, v167, v217
	v_add_f32_e32 v102, v198, v248
	s_branch .LBB0_1280
